# stack2 + plain (unscaled) f8f6f4 MFMA form for all unit-scale MX MFMAs
# baseline (speedup 1.0000x reference)
.LBB0_565:
	s_waitcnt lgkmcnt(4)
	v_mfma_f32_32x32x64_f8f6f4 v[96:111], v[96:103], v[120:127], 0
	v_fma_f32 v80, v80, s40, -v192
	v_fma_f32 v81, v81, s40, -v192
	v_fma_f32 v84, v84, s40, -v192
	v_fma_f32 v85, v85, s40, -v192
	v_fma_f32 v88, v88, s40, -v192
	v_fma_f32 v89, v89, s40, -v192
	v_fma_f32 v92, v92, s40, -v192
	v_fma_f32 v93, v93, s40, -v192
	v_exp_f32_e32 v80, v80
	v_exp_f32_e32 v81, v81
	v_exp_f32_e32 v84, v84
	v_exp_f32_e32 v85, v85
	v_exp_f32_e32 v88, v88
	v_exp_f32_e32 v89, v89
	s_waitcnt lgkmcnt(2)
	v_mfma_f32_32x32x64_f8f6f4 v[96:111], v[156:163], v[128:135], v[96:111]
	v_exp_f32_e32 v92, v92
	v_exp_f32_e32 v93, v93
	v_fma_f32 v82, v82, s40, -v192
	v_fma_f32 v83, v83, s40, -v192
	v_fma_f32 v86, v86, s40, -v192
	v_fma_f32 v87, v87, s40, -v192
	v_fma_f32 v90, v90, s40, -v192
	v_fma_f32 v91, v91, s40, -v192
	v_fma_f32 v94, v94, s40, -v192
	v_fma_f32 v95, v95, s40, -v192
	v_exp_f32_e32 v82, v82
	v_exp_f32_e32 v83, v83
	v_exp_f32_e32 v86, v86
	v_exp_f32_e32 v87, v87
	v_exp_f32_e32 v90, v90
	s_waitcnt lgkmcnt(0)
	v_mfma_f32_32x32x64_f8f6f4 v[96:111], v[148:155], v[136:143], v[96:111]
	v_lshl_add_u32 v240, s23, 14, v211
	ds_read_b128 v[224:227], v240
	ds_read_b128 v[228:231], v240 offset:16
	ds_read_b128 v[232:235], v240 offset:2560
	ds_read_b128 v[236:239], v240 offset:2576
	v_exp_f32_e32 v91, v91
	v_exp_f32_e32 v94, v94
	v_exp_f32_e32 v95, v95
	v_cvt_pk_fp8_f32 v148, v80, v81
	v_cvt_pk_fp8_f32 v149, v84, v85
	v_cvt_pk_fp8_f32 v150, v88, v89
	v_cvt_pk_fp8_f32 v151, v92, v93
	v_cvt_pk_fp8_f32 v148, v82, v83 op_sel:[0,0,1]
	v_cvt_pk_fp8_f32 v149, v86, v87 op_sel:[0,0,1]
	v_cvt_pk_fp8_f32 v150, v90, v91 op_sel:[0,0,1]
	v_cvt_pk_fp8_f32 v151, v94, v95 op_sel:[0,0,1]
	s_nop 0
	s_waitcnt lgkmcnt(2)
	v_mfma_f32_32x32x64_f8f6f4 v[48:63], v[144:151], v[224:231], v[48:63]
	ds_read_b128 v[80:83], v240 offset:5120
	ds_read_b128 v[84:87], v240 offset:5136
	ds_read_b128 v[152:155], v240 offset:7680
	ds_read_b128 v[156:159], v240 offset:7696
	s_waitcnt lgkmcnt(4)
	v_mfma_f32_32x32x64_f8f6f4 v[32:47], v[144:151], v[232:239], v[32:47]
	v_max_f32_e32 v88, v96, v97
	v_max3_f32 v88, v88, v98, v99
	v_max3_f32 v88, v88, v100, v101
	v_max3_f32 v88, v88, v102, v103
	v_max3_f32 v88, v88, v104, v105
	v_max3_f32 v88, v88, v106, v107
	s_waitcnt lgkmcnt(2)
	v_mfma_f32_32x32x64_f8f6f4 v[16:31], v[144:151], v[80:87], v[16:31]
	v_max3_f32 v88, v88, v108, v109
	v_max3_f32 v88, v88, v110, v111
	v_mov_b32_e32 v89, v88
	s_nop 1
	v_permlane32_swap_b32_e32 v88, v89
	v_max_f32_e32 v80, v88, v89
	v_fma_f32 v81, v80, s40, -v192
	v_cmp_ge_f32_e32 vcc, s70, v81
	s_waitcnt lgkmcnt(0)
	v_mfma_f32_32x32x64_f8f6f4 v[0:15], v[144:151], v[152:159], v[0:15]
	s_cmp_eq_u64 vcc, exec
	s_cbranch_scc0 .Lmla_rare_a0
	v_mov_b32_e32 v88, 1.0

.LBB0_570:
	s_waitcnt lgkmcnt(4)
	v_mfma_f32_32x32x64_f8f6f4 v[80:95], v[80:87], v[120:127], 0
	s_cmp_ge_u32 s18, s20
	s_waitcnt lgkmcnt(2)
	v_mfma_f32_32x32x64_f8f6f4 v[80:95], v[104:111], v[128:135], v[80:95]
	s_waitcnt lgkmcnt(0)
	v_mfma_f32_32x32x64_f8f6f4 v[80:95], v[96:103], v[136:143], v[80:95]
	s_nop 15
	s_nop 3
	v_max_f32_e32 v96, v80, v81
	v_max3_f32 v96, v96, v82, v83
	v_max3_f32 v96, v96, v84, v85
	v_max3_f32 v96, v96, v86, v87
	v_max3_f32 v96, v96, v88, v89
	v_max3_f32 v96, v96, v90, v91
	v_max3_f32 v96, v96, v92, v93
	v_max3_f32 v96, v96, v94, v95
	v_mov_b32_e32 v97, v96
	s_nop 1
	v_permlane32_swap_b32_e32 v96, v97
	v_max_f32_e32 v96, v96, v97
	v_fma_f32 v97, v96, s40, -v192
	v_cmp_ge_f32_e32 vcc, s70, v97
	s_cbranch_scc1 .LBB0_577
	s_xor_b32 s25, s23, 1
	s_lshl_b32 s18, s25, 15
	s_add_i32 s26, s18, 0
	v_add3_u32 v97, s26, v212, v190
	s_waitcnt vmcnt(1)
	ds_write_b128 v97, v[168:171]
	s_and_saveexec_b64 s[18:19], s[0:1]
	v_add3_u32 v97, s26, v215, v188
	ds_write_b128 v97, v[164:167]
	s_or_b64 exec, exec, s[18:19]
	v_lshl_add_u32 v97, s25, 14, v207
	s_cmp_ge_u32 s78, s74
	s_waitcnt vmcnt(0)
	ds_write_b128 v97, v[172:175]
	s_cbranch_scc1 .LBB0_577
	s_cmp_lt_u32 s78, s77
	s_cselect_b32 s18, 0, s77
	s_cselect_b32 s19, s76, s75
	s_lshl_b32 s18, s18, 6
	s_sub_i32 s25, s19, s18
	s_add_i32 s25, s25, s22
	v_add_u32_e32 v97, s25, v210
	v_mad_i64_i32 v[98:99], s[18:19], v97, s64, v[194:195]
	global_load_dwordx4 v[168:171], v[98:99], off
	s_and_saveexec_b64 s[18:19], s[0:1]
	s_cbranch_execz .LBB0_576
	v_add_u32_e32 v97, s25, v213
	v_mad_i64_i32 v[98:99], s[26:27], v97, s64, v[196:197]
	global_load_dwordx4 v[164:167], v[98:99], off

.LBB0_1875:
	s_waitcnt lgkmcnt(4)
	v_mfma_f32_32x32x64_f8f6f4 v[96:111], v[96:103], v[120:127], 0
	v_fma_f32 v80, v80, s38, -v194
	v_fma_f32 v81, v81, s38, -v194
	v_fma_f32 v84, v84, s38, -v194
	v_fma_f32 v85, v85, s38, -v194
	v_fma_f32 v88, v88, s38, -v194
	v_fma_f32 v89, v89, s38, -v194
	v_fma_f32 v92, v92, s38, -v194
	v_fma_f32 v93, v93, s38, -v194
	v_exp_f32_e32 v80, v80
	v_exp_f32_e32 v81, v81
	v_exp_f32_e32 v84, v84
	v_exp_f32_e32 v85, v85
	v_exp_f32_e32 v88, v88
	v_exp_f32_e32 v89, v89
	s_waitcnt lgkmcnt(2)
	v_mfma_f32_32x32x64_f8f6f4 v[96:111], v[156:163], v[128:135], v[96:111]
	v_exp_f32_e32 v92, v92
	v_exp_f32_e32 v93, v93
	v_fma_f32 v82, v82, s38, -v194
	v_fma_f32 v83, v83, s38, -v194
	v_fma_f32 v86, v86, s38, -v194
	v_fma_f32 v87, v87, s38, -v194
	v_fma_f32 v90, v90, s38, -v194
	v_fma_f32 v91, v91, s38, -v194
	v_fma_f32 v94, v94, s38, -v194
	v_fma_f32 v95, v95, s38, -v194
	v_exp_f32_e32 v82, v82
	v_exp_f32_e32 v83, v83
	v_exp_f32_e32 v86, v86
	v_exp_f32_e32 v87, v87
	v_exp_f32_e32 v90, v90
	s_waitcnt lgkmcnt(0)
	v_mfma_f32_32x32x64_f8f6f4 v[96:111], v[148:155], v[136:143], v[96:111]
	v_lshl_add_u32 v240, s24, 14, v209
	ds_read_b128 v[224:227], v240
	ds_read_b128 v[228:231], v240 offset:16
	ds_read_b128 v[232:235], v240 offset:2560
	ds_read_b128 v[236:239], v240 offset:2576
	v_exp_f32_e32 v91, v91
	v_exp_f32_e32 v94, v94
	v_exp_f32_e32 v95, v95
	v_cvt_pk_fp8_f32 v148, v80, v81
	v_cvt_pk_fp8_f32 v149, v84, v85
	v_cvt_pk_fp8_f32 v150, v88, v89
	v_cvt_pk_fp8_f32 v151, v92, v93
	v_cvt_pk_fp8_f32 v148, v82, v83 op_sel:[0,0,1]
	v_cvt_pk_fp8_f32 v149, v86, v87 op_sel:[0,0,1]
	v_cvt_pk_fp8_f32 v150, v90, v91 op_sel:[0,0,1]
	v_cvt_pk_fp8_f32 v151, v94, v95 op_sel:[0,0,1]
	s_nop 0
	s_waitcnt lgkmcnt(2)
	v_mfma_f32_32x32x64_f8f6f4 v[48:63], v[144:151], v[224:231], v[48:63]
	ds_read_b128 v[80:83], v240 offset:5120
	ds_read_b128 v[84:87], v240 offset:5136
	ds_read_b128 v[152:155], v240 offset:7680
	ds_read_b128 v[156:159], v240 offset:7696
	s_waitcnt lgkmcnt(4)
	v_mfma_f32_32x32x64_f8f6f4 v[32:47], v[144:151], v[232:239], v[32:47]
	v_max_f32_e32 v88, v96, v97
	v_max3_f32 v88, v88, v98, v99
	v_max3_f32 v88, v88, v100, v101
	v_max3_f32 v88, v88, v102, v103
	v_max3_f32 v88, v88, v104, v105
	v_max3_f32 v88, v88, v106, v107
	s_waitcnt lgkmcnt(2)
	v_mfma_f32_32x32x64_f8f6f4 v[16:31], v[144:151], v[80:87], v[16:31]
	v_max3_f32 v88, v88, v108, v109
	v_max3_f32 v88, v88, v110, v111
	v_mov_b32_e32 v89, v88
	s_nop 1
	v_permlane32_swap_b32_e32 v88, v89
	v_max_f32_e32 v80, v88, v89
	v_fma_f32 v81, v80, s38, -v194
	v_cmp_ge_f32_e32 vcc, s68, v81
	s_waitcnt lgkmcnt(0)
	v_mfma_f32_32x32x64_f8f6f4 v[0:15], v[144:151], v[152:159], v[0:15]
	s_cmp_eq_u64 vcc, exec
	s_cbranch_scc0 .Lmla_rare_a1
	v_mov_b32_e32 v88, 1.0
